# v17 = v16 + GLA-prep unit order with the 64 cheap context chunks last (balances the fifth round)
# baseline (speedup 1.0000x reference)
; __device__ __forceinline__ int ptid() { int t = threadIdx.x; asm volatile("" : "+v"(t)); return t; }
; __device__ __forceinline__ void ph_glaprep(const Params& p, float* lds, int wg, int nwg) {
;     bf16_t* Qs = (bf16_t*)lds;
;     bf16_t* Ks = Qs + 64 * GLA_LDP;
;     float* lrs = (float*)(Ks + 64 * GLA_LDP);
;     float* hsum = lrs + 64 * 16;
;     const int tid = ptid(), wave = __builtin_amdgcn_readfirstlane(tid >> 6), lane = tid & 63;
;     for (int unit = wg; unit < 16 * GLA_NCH; unit += nwg) {
;         const int bhd = unit / GLA_NCH, c = unit % GLA_NCH;
;         const int b = bhd >> 3, h = (bhd >> 1) & 3, dir = bhd & 1;
;         const bool isctx = c < 4;
;         const int T = isctx ? TC : TL, base = isctx ? NL + b * TC : b * TL, cc = isctx ? c : c - 4;
;         for (int q = tid; q < 64 * 16; q += NTHR) { const int i = q >> 4, j = q & 15, idx = cc * 64 + i, t = dir ? T - 1 - idx : idx;
;             lrs[q] = p.LRs[(size_t)(base + t) * 256 + 16 * dir + j]; }
; #pragma unroll
;         for (int q4 = 0; q4 < 4; ++q4) { const int e = tid + q4 * NTHR, i = e >> 5, c8 = e & 31, idx = cc * 64 + i, t = dir ? T - 1 - idx : idx;
;             const bf16_t* pr = p.P + (size_t)(base + t) * L1LD + h * 256 + c8 * 8;
;             *(uint4*)(Ks + i * GLA_LDP + c8 * 8) = *(const uint4*)pr;
;             if (!isctx) *(uint4*)(Qs + i * GLA_LDP + c8 * 8) = *(const uint4*)(pr + 3104); }
.LBB0_1442:
	s_or_b64 exec, exec, s[0:1]
	v_mov_b32_e32 v34, v0
	s_waitcnt lgkmcnt(0)
	s_barrier
	s_and_b64 vcc, exec, s[92:93]
	v_readfirstlane_b32 s0, v34
	s_cbranch_vccz .LBB0_1541
	s_movk_i32 s1, 0x400
	v_cmp_gt_i32_e64 s[6:7], s1, v34
	v_and_b32_e32 v38, 0xff, v34
	v_lshlrev_b32_e32 v41, 2, v34
	s_add_i32 s1, 0, 0x11800
	v_add_u32_e32 v73, s1, v41
	v_lshl_add_u32 v75, v38, 2, s1
	s_movk_i32 s1, 0x100
	v_lshlrev_b32_e32 v3, 3, v34
	v_cmp_gt_u32_e64 s[8:9], s1, v34
	v_and_b32_e32 v14, 15, v34
	s_movk_i32 s1, 0xff80
	v_and_b32_e32 v2, 0xf8, v3
	v_and_or_b32 v8, v3, s1, v14
	v_bfe_u32 v3, v34, 4, 2
	s_lshr_b32 s1, s0, 5
	s_ashr_i32 s2, s0, 7
	s_and_b32 s3, s1, 2
	v_lshlrev_b32_e32 v16, 2, v3
	v_lshl_add_u32 v10, v3, 4, 0
	v_add_u32_e32 v3, 0x400, v34
	v_ashrrev_i32_e32 v5, 8, v34
	v_bfe_u32 v11, v34, 5, 3
	v_lshl_or_b32 v15, s2, 4, v14
	s_and_b32 s0, s0, 0xffffff80
	s_lshl_b32 s1, s3, 5
	s_movk_i32 s5, 0x210
	v_ashrrev_i32_e32 v79, 5, v3
	v_add_u32_e32 v3, 0x600, v34
	s_or_b32 s4, s1, s0
	v_mad_u64_u32 v[42:43], s[0:1], v15, s5, v[10:11]
	v_add_u32_e32 v47, 0x200, v34
	v_ashrrev_i32_e32 v81, 5, v3
	v_mul_i32_i24_e32 v3, 0x2100, v5
	v_readlane_b32 s12, v246, 16
	v_mov_b32_e32 v37, 0
	v_lshl_add_u32 v4, v2, 1, 0
	v_lshlrev_b32_e32 v6, 1, v34
	v_ashrrev_i32_e32 v43, 5, v34
	v_ashrrev_i32_e32 v77, 5, v47
	v_or_b32_e32 v3, v3, v38
	v_lshlrev_b32_e32 v36, 2, v14
	v_readlane_b32 s13, v246, 17
	v_readlane_b32 s14, v246, 18
	v_readlane_b32 s15, v246, 19
	v_readlane_b32 s16, v246, 20
	v_readlane_b32 s17, v246, 21
	v_readlane_b32 s18, v246, 22
	v_readlane_b32 s19, v246, 23
	v_readlane_b32 s20, v246, 24
	v_readlane_b32 s21, v246, 25
	v_readlane_b32 s22, v246, 26
	v_readlane_b32 s23, v246, 27
	v_readlane_b32 s24, v246, 28
	v_readlane_b32 s25, v246, 29
	v_readlane_b32 s26, v246, 30
	v_readlane_b32 s27, v246, 31
	v_and_b32_e32 v12, 48, v6
	v_mad_u64_u32 v[44:45], s[0:1], v43, s5, v[4:5]
	v_mad_u64_u32 v[48:49], s[0:1], v77, s5, v[4:5]
	v_mad_u64_u32 v[50:51], s[0:1], v79, s5, v[4:5]
	v_mad_u64_u32 v[52:53], s[0:1], v81, s5, v[4:5]
	v_lshl_add_u32 v83, v3, 1, 0
	v_lshlrev_b32_e32 v3, 10, v5
	v_lshlrev_b32_e32 v4, 6, v11
	v_lshl_add_u64 v[58:59], s[16:17], 0, v[36:37]
	v_readlane_b32 s12, v248, 9
	s_add_i32 s51, 0, 0x10800
	v_lshrrev_b32_e32 v6, 3, v34
	v_or3_b32 v3, v4, v3, v12
	v_readlane_b32 s13, v248, 10
	v_readlane_b32 s14, v248, 11
	v_readlane_b32 s15, v248, 12
	v_readlane_b32 s16, v248, 13
	v_readlane_b32 s17, v248, 14
	v_readlane_b32 s18, v248, 15
	v_readlane_b32 s19, v248, 16
	v_readlane_b32 s20, v248, 17
	v_readlane_b32 s21, v248, 18
	v_readlane_b32 s22, v248, 19
	v_readlane_b32 s23, v248, 20
	v_lshl_add_u32 v39, v5, 11, s51
	v_and_b32_e32 v13, 7, v34
	v_and_b32_e32 v6, 30, v6
	v_lshlrev_b32_e32 v54, 3, v3
	v_lshl_or_b32 v3, v5, 5, 16
	s_movk_i32 s0, 0x108
	v_readlane_b32 s24, v248, 21
	v_readlane_b32 s25, v248, 22
	v_readlane_b32 s26, v248, 23
	v_readlane_b32 s27, v248, 24
	s_mov_b64 s[12:13], s[16:17]
	v_add_u32_e32 v6, v6, v5
	v_mad_u64_u32 v[4:5], s[0:1], v3, s0, v[38:39]
	s_cmp_le_i32 s3, s2
	v_lshlrev_b32_e32 v36, 1, v13
	s_mov_b64 s[14:15], s[18:19]
	s_mov_b64 s[16:17], s[20:21]
	s_mov_b64 s[18:19], s[22:23]
	v_lshl_or_b32 v6, v6, 6, v14
	s_cselect_b64 s[46:47], -1, 0
	s_lshl_b32 s0, s3, 4
	s_mov_b64 s[20:21], s[24:25]
	s_mov_b64 s[22:23], s[26:27]
	v_lshl_add_u64 v[60:61], s[18:19], 0, v[36:37]
	v_readlane_b32 s12, v248, 29
	v_ashrrev_i32_e32 v7, 31, v6
	v_ashrrev_i32_e32 v9, 31, v8
	v_readlane_b32 s13, v248, 30
	v_or_b32_e32 v5, s0, v16
	v_lshl_add_u64 v[62:63], v[6:7], 4, s[20:21]
	v_readlane_b32 s16, v248, 33
	v_readlane_b32 s17, v248, 34
	v_lshl_add_u64 v[64:65], v[8:9], 4, s[12:13]
	v_cmp_gt_i32_e64 s[10:11], v5, v15
	v_cmp_lt_i32_e64 s[12:13], v5, v15
	v_or_b32_e32 v6, 2, v5
	v_or_b32_e32 v5, 3, v5
	v_cmp_gt_i32_e64 s[16:17], v5, v15
	v_lshrrev_b32_e32 v5, 1, v34
	s_cmp_lt_i32 s3, s2
	v_and_b32_e32 v5, 16, v5
	s_cselect_b64 s[48:49], -1, 0
	s_or_b32 s1, s0, 16
	v_or3_b32 v5, v14, v5, s4
	v_readlane_b32 s14, v248, 31
	v_readlane_b32 s15, v248, 32
	v_lshlrev_b32_e32 v66, 3, v5
	v_or_b32_e32 v5, s1, v16
	v_readlane_b32 s18, v248, 35
	v_readlane_b32 s19, v248, 36
	v_cmp_gt_i32_e64 s[14:15], v6, v15
	v_or_b32_e32 v6, 2, v5
	v_cmp_gt_i32_e64 s[18:19], v5, v15
	v_cmp_lt_i32_e64 s[20:21], v5, v15
	v_cmp_gt_i32_e64 s[22:23], v6, v15
	v_or_b32_e32 v6, 3, v5
	v_lshlrev_b32_e32 v5, 1, v5
	v_and_b32_e32 v5, 48, v5
	v_or3_b32 v5, v14, v5, s4
	v_lshlrev_b32_e32 v68, 3, v5
	v_max_i32_e32 v5, 0x200, v34
	v_sub_u32_e32 v5, v5, v34
	v_add_u32_e32 v5, 0x1ff, v5
	v_cmp_gt_i32_e64 s[24:25], v6, v15
	v_lshrrev_b32_e32 v6, 9, v5
	v_lshrrev_b32_e32 v3, 1, v3
	v_add_u32_e32 v7, 1, v6
	v_add_u32_e32 v6, -1, v6
	v_lshl_add_u32 v84, v4, 1, 0
	v_or_b32_e32 v3, v3, v11
	v_lshlrev_b32_e32 v4, 3, v12
	s_movk_i32 s56, 0x1ff
	v_lshrrev_b32_e32 v8, 1, v6
	v_lshl_or_b32 v56, v3, 9, v4
	v_or_b32_e32 v3, s0, v14
	v_or_b32_e32 v4, s1, v14
	v_add_u32_e32 v8, 1, v8
	v_cmp_lt_u32_e64 s[26:27], s56, v5
	v_and_b32_e32 v5, 0xfffffe, v7
	v_ashrrev_i32_e32 v35, 31, v34
	v_mul_u32_u24_e32 v3, 0x210, v3
	v_mul_u32_u24_e32 v4, 0x210, v4
	v_lshl_add_u32 v100, v5, 9, v34
	v_and_b32_e32 v101, 3, v8
	v_cmp_ne_u32_e64 s[34:35], v7, v5
	v_add_u32_e32 v5, 0, v41
	s_mov_b32 s41, 0
	v_and_b32_e32 v40, 4, v16
	v_add_u32_e32 v45, 0x8400, v44
	v_add_u32_e32 v49, 0x8400, v48
	v_add_u32_e32 v51, 0x8400, v50
	v_add_u32_e32 v53, 0x8400, v52
	v_ashrrev_i32_e32 v55, 31, v54
	v_ashrrev_i32_e32 v57, 31, v56
	v_add_u32_e32 v85, 0x210, v84
	v_add_u32_e32 v86, 0x420, v84
	v_add_u32_e32 v87, 0x630, v84
	v_add_u32_e32 v88, 0x840, v84
	v_add_u32_e32 v89, 0xa50, v84
	v_add_u32_e32 v90, 0xc60, v84
	v_add_u32_e32 v91, 0xe70, v84
	v_add_u32_e32 v92, 0x1080, v84
	v_add_u32_e32 v93, 0x1290, v84
	v_add_u32_e32 v94, 0x14a0, v84
	v_add_u32_e32 v95, 0x16b0, v84
	v_add_u32_e32 v96, 0x18c0, v84
	v_add_u32_e32 v97, 0x1ad0, v84
	v_add_u32_e32 v98, 0x1ce0, v84
	v_add_u32_e32 v99, 0x1ef0, v84
	v_ashrrev_i32_e32 v67, 31, v66
	v_ashrrev_i32_e32 v69, 31, v68
	v_mov_b32_e32 v46, v34
	v_cmp_lt_u32_e64 s[28:29], 5, v6
	v_and_b32_e32 v102, -4, v8
	v_cmp_ne_u32_e64 s[30:31], 0, v101
	v_add_u32_e32 v103, 0x10800, v5
	v_add_u32_e32 v104, 0x11000, v5
	s_movk_i32 s57, 0x3200
	v_lshlrev_b32_e32 v36, 1, v2
	s_mov_b32 s58, 0x800000
	s_mov_b32 s59, 0x3f317217
	s_mov_b32 s60, 0x7f800000
	s_mov_b32 s61, 0xc1a00000
	s_mov_b32 s50, 0xbd800000
	v_lshlrev_b64 v[70:71], 1, v[34:35]
	v_add_u32_e32 v35, v10, v3
	v_add_u32_e32 v105, v10, v4
	v_mov_b32_e32 v106, 0x41b17218
	s_mov_b32 s80, s90
	s_branch .LBB0_1446

; __device__ __forceinline__ void ph_glaprep(const Params& p, float* lds, int wg, int nwg) {
;     ...
;     for (int unit = wg; unit < 16 * GLA_NCH; unit += nwg) {
;         const int bhd = unit / GLA_NCH, c = unit % GLA_NCH;
;         const int b = bhd >> 3, h = (bhd >> 1) & 3, dir = bhd & 1;
;         const bool isctx = c < 4;
;         const int T = isctx ? TC : TL, base = isctx ? NL + b * TC : b * TL, cc = isctx ? c : c - 4;
.LBB0_1445:
	s_add_i32 s80, s80, s96
	s_cmpk_lt_i32 s80, 0x440
	s_barrier
	s_cbranch_scc0 .LBB0_1540
.LBB0_1446:
	s_cmpk_lt_i32 s80, 0x400
	s_cbranch_scc0 .Lgp_ctx
	s_lshr_b32 s0, s80, 6
	s_and_b32 s1, s80, 63
	s_add_i32 s1, s1, 4
	s_branch .Lgp_join
.Lgp_ctx:
	s_sub_i32 s1, s80, 0x400
	s_lshr_b32 s0, s1, 2
	s_and_b32 s1, s1, 3
.Lgp_join:
	s_mul_i32 s0, s0, 0x44
	s_add_i32 s52, s0, s1
	s_mul_hi_i32 s0, s52, 0x78787879
	s_lshr_b32 s1, s0, 31
	s_ashr_i32 s5, s0, 5
	s_add_i32 s5, s5, s1
	s_mul_i32 s0, s5, 0x44
	s_sub_i32 s0, s52, s0
	s_ashr_i32 s1, s5, 3
	s_and_b32 s4, s5, 1
	s_cmp_gt_i32 s0, 3
	s_cselect_b64 s[42:43], -1, 0
	s_lshl_b32 s2, s1, 8
	s_lshl_b32 s33, s0, 6
	s_addk_i32 s2, 0x2000
	s_lshl_b32 s1, s1, 12
	s_add_i32 s36, s33, 0xffffff00
	s_cmp_lt_i32 s0, 4
	s_movk_i32 s0, 0x1000
	s_cselect_b32 s3, 0x100, s0
	s_cselect_b32 s2, s2, s1
	s_cselect_b32 s33, s33, s36
	s_and_saveexec_b64 s[36:37], s[6:7]
	s_cbranch_execz .LBB0_1461
	s_cmp_eq_u32 s4, 0
	s_cselect_b64 vcc, -1, 0
	s_lshl_b32 s40, s4, 6
	v_lshl_add_u64 v[2:3], v[58:59], 0, s[40:41]
	s_mov_b64 s[0:1], -1
	v_mov_b32_e32 v4, v34
	v_mov_b32_e32 v5, v41
	s_and_saveexec_b64 s[38:39], s[26:27]
	s_cbranch_execz .LBB0_1458
	v_mov_b32_e32 v8, 0
	v_mov_b64_e32 v[4:5], v[46:47]
	s_and_saveexec_b64 s[44:45], s[28:29]
	s_cbranch_execz .LBB0_1452
	s_mov_b32 s40, 0
	s_mov_b64 s[54:55], 0
	v_mov_b32_e32 v6, v102
	v_mov_b32_e32 v7, v103
	v_mov_b64_e32 v[4:5], v[46:47]
